# M2 epilogue operands prefetched: bias loads at unit header into free VGPRs, gates from an LDS gate cache filled at moe_setup; epilogue has no global load wait
# baseline (speedup 1.0000x reference)
.LBB0_2942:
	s_or_b64 exec, exec, s[6:7]
	v_readlane_b32 s4, v255, 6
	s_waitcnt lgkmcnt(0)
	s_barrier
	v_mov_b32_e32 v2, s4
	ds_read_b32 v2, v2
	s_waitcnt lgkmcnt(0)
	v_lshlrev_b32_e32 v7, 8, v2
	v_cmp_lt_i32_e32 vcc, v6, v7
	s_and_saveexec_b64 s[6:7], vcc
	s_cbranch_execz .LBB0_2947
	s_add_u32 s8, s14, 0x49cfe000
	v_readlane_b32 s4, v254, 39
	s_addc_u32 s9, s15, 0
	v_and_b32_e32 v8, 0xff, v6
	s_mov_b32 s11, 0x23000
	v_lshl_add_u32 v9, v6, 2, s4
	v_lshrrev_b32_e32 v10, 8, v6
	v_lshlrev_b32_e32 v10, 4, v10
	v_add_u32_e32 v10, 0x23000, v10
	ds_read2_b32 v[24:25], v10 offset0:128 offset1:130
	ds_read2_b32 v[26:27], v10 offset0:136 offset1:138
	ds_read2_b32 v[28:29], v10 offset0:144 offset1:146
	ds_read2_b32 v[30:31], v10 offset0:152 offset1:154
	ds_read2_b32 v[32:33], v10 offset0:160 offset1:162
	ds_read2_b32 v[34:35], v10 offset0:168 offset1:170
	s_waitcnt lgkmcnt(0)
	v_cmp_lt_i32_e32 vcc, v6, v7
	s_nop 1
	v_cndmask_b32_e32 v48, 0, v25, vcc
	v_cndmask_b32_e32 v24, 0, v24, vcc
	v_cndmask_b32_e64 v54, -1, 0, vcc
	v_lshl_add_u32 v72, v48, 2, s11
	ds_read2_b32 v[36:37], v72 offset1:32
	v_add_u32_e32 v78, 512, v6
	v_cmp_lt_i32_e32 vcc, v78, v7
	s_nop 1
	v_cndmask_b32_e32 v49, 0, v27, vcc
	v_cndmask_b32_e32 v26, 0, v26, vcc
	v_cndmask_b32_e64 v55, -1, 0, vcc
	v_lshl_add_u32 v73, v49, 2, s11
	ds_read2_b32 v[38:39], v73 offset1:32
	v_add_u32_e32 v78, 1024, v6
	v_cmp_lt_i32_e32 vcc, v78, v7
	s_nop 1
	v_cndmask_b32_e32 v50, 0, v29, vcc
	v_cndmask_b32_e32 v28, 0, v28, vcc
	v_cndmask_b32_e64 v56, -1, 0, vcc
	v_lshl_add_u32 v74, v50, 2, s11
	ds_read2_b32 v[40:41], v74 offset1:32
	v_add_u32_e32 v78, 1536, v6
	v_cmp_lt_i32_e32 vcc, v78, v7
	s_nop 1
	v_cndmask_b32_e32 v51, 0, v31, vcc
	v_cndmask_b32_e32 v30, 0, v30, vcc
	v_cndmask_b32_e64 v57, -1, 0, vcc
	v_lshl_add_u32 v75, v51, 2, s11
	ds_read2_b32 v[42:43], v75 offset1:32
	v_add_u32_e32 v78, 2048, v6
	v_cmp_lt_i32_e32 vcc, v78, v7
	s_nop 1
	v_cndmask_b32_e32 v52, 0, v33, vcc
	v_cndmask_b32_e32 v32, 0, v32, vcc
	v_cndmask_b32_e64 v58, -1, 0, vcc
	v_lshl_add_u32 v76, v52, 2, s11
	ds_read2_b32 v[44:45], v76 offset1:32
	v_add_u32_e32 v78, 2560, v6
	v_cmp_lt_i32_e32 vcc, v78, v7
	s_nop 1
	v_cndmask_b32_e32 v53, 0, v35, vcc
	v_cndmask_b32_e32 v34, 0, v34, vcc
	v_cndmask_b32_e64 v59, -1, 0, vcc
	v_lshl_add_u32 v77, v53, 2, s11
	ds_read2_b32 v[46:47], v77 offset1:32
	s_waitcnt lgkmcnt(0)
	v_sub_u32_e32 v60, v24, v37
	v_lshl_or_b32 v60, v60, 8, v8
	v_cmp_lt_i32_e32 vcc, v60, v36
	v_mul_u32_u24_e32 v72, 0x11000, v48
	s_nop 0
	v_cndmask_b32_e32 v60, 0, v60, vcc
	v_cndmask_b32_e64 v79, -1, 0, vcc
	v_or_b32_e32 v54, v54, v79
	v_lshl_add_u32 v60, v60, 2, v72
	global_load_dword v66, v60, s[8:9]
	v_sub_u32_e32 v61, v26, v39
	v_lshl_or_b32 v61, v61, 8, v8
	v_cmp_lt_i32_e32 vcc, v61, v38
	v_mul_u32_u24_e32 v73, 0x11000, v49
	s_nop 0
	v_cndmask_b32_e32 v61, 0, v61, vcc
	v_cndmask_b32_e64 v79, -1, 0, vcc
	v_or_b32_e32 v55, v55, v79
	v_lshl_add_u32 v61, v61, 2, v73
	global_load_dword v67, v61, s[8:9]
	v_sub_u32_e32 v62, v28, v41
	v_lshl_or_b32 v62, v62, 8, v8
	v_cmp_lt_i32_e32 vcc, v62, v40
	v_mul_u32_u24_e32 v74, 0x11000, v50
	s_nop 0
	v_cndmask_b32_e32 v62, 0, v62, vcc
	v_cndmask_b32_e64 v79, -1, 0, vcc
	v_or_b32_e32 v56, v56, v79
	v_lshl_add_u32 v62, v62, 2, v74
	global_load_dword v68, v62, s[8:9]
	v_sub_u32_e32 v63, v30, v43
	v_lshl_or_b32 v63, v63, 8, v8
	v_cmp_lt_i32_e32 vcc, v63, v42
	v_mul_u32_u24_e32 v75, 0x11000, v51
	s_nop 0
	v_cndmask_b32_e32 v63, 0, v63, vcc
	v_cndmask_b32_e64 v79, -1, 0, vcc
	v_or_b32_e32 v57, v57, v79
	v_lshl_add_u32 v63, v63, 2, v75
	global_load_dword v69, v63, s[8:9]
	v_sub_u32_e32 v64, v32, v45
	v_lshl_or_b32 v64, v64, 8, v8
	v_cmp_lt_i32_e32 vcc, v64, v44
	v_mul_u32_u24_e32 v76, 0x11000, v52
	s_nop 0
	v_cndmask_b32_e32 v64, 0, v64, vcc
	v_cndmask_b32_e64 v79, -1, 0, vcc
	v_or_b32_e32 v58, v58, v79
	v_lshl_add_u32 v64, v64, 2, v76
	global_load_dword v70, v64, s[8:9]
	v_sub_u32_e32 v65, v34, v47
	v_lshl_or_b32 v65, v65, 8, v8
	v_cmp_lt_i32_e32 vcc, v65, v46
	v_mul_u32_u24_e32 v77, 0x11000, v53
	s_nop 0
	v_cndmask_b32_e32 v65, 0, v65, vcc
	v_cndmask_b32_e64 v79, -1, 0, vcc
	v_or_b32_e32 v59, v59, v79
	v_lshl_add_u32 v65, v65, 2, v77
	global_load_dword v71, v65, s[8:9]
	s_waitcnt vmcnt(0)
	v_or_b32_e32 v66, v66, v54
	ds_write_b32 v9, v66
	v_or_b32_e32 v67, v67, v55
	ds_write_b32 v9, v67 offset:2048
	v_or_b32_e32 v68, v68, v56
	ds_write_b32 v9, v68 offset:4096
	v_or_b32_e32 v69, v69, v57
	ds_write_b32 v9, v69 offset:6144
	v_or_b32_e32 v70, v70, v58
	ds_write_b32 v9, v70 offset:8192
	v_or_b32_e32 v71, v71, v59
	ds_write_b32 v9, v71 offset:10240
	s_add_u32 s8, s14, 0x49cba000
	s_addc_u32 s9, s15, 0
	v_max_i32_e32 v72, 0, v66
	v_lshlrev_b32_e32 v72, 2, v72
	global_load_dword v60, v72, s[8:9]
	v_max_i32_e32 v73, 0, v67
	v_lshlrev_b32_e32 v73, 2, v73
	global_load_dword v61, v73, s[8:9]
	v_max_i32_e32 v74, 0, v68
	v_lshlrev_b32_e32 v74, 2, v74
	global_load_dword v62, v74, s[8:9]
	v_max_i32_e32 v75, 0, v69
	v_lshlrev_b32_e32 v75, 2, v75
	global_load_dword v63, v75, s[8:9]
	v_max_i32_e32 v76, 0, v70
	v_lshlrev_b32_e32 v76, 2, v76
	global_load_dword v64, v76, s[8:9]
	v_max_i32_e32 v77, 0, v71
	v_lshlrev_b32_e32 v77, 2, v77
	global_load_dword v65, v77, s[8:9]
	s_waitcnt vmcnt(0)
	ds_write_b32 v9, v60 offset:13568
	ds_write_b32 v9, v61 offset:15616
	ds_write_b32 v9, v62 offset:17664
	ds_write_b32 v9, v63 offset:19712
	ds_write_b32 v9, v64 offset:21760
	ds_write_b32 v9, v65 offset:23808

.LBB0_2955:
	v_ashrrev_i32_e32 v143, 31, v22
	v_mov_b32_e32 v142, v22
	v_lshlrev_b64 v[142:143], 12, v[142:143]
	v_lshl_add_u64 v[144:145], s[8:9], 0, v[142:143]
	v_lshl_or_b32 v142, v23, 8, v164
	v_ashrrev_i32_e32 v143, 31, v142
	v_lshl_add_u64 v[142:143], v[142:143], 2, v[144:145]
	global_load_dwordx4 v[242:245], v[142:143], off offset:16
	global_load_dwordx4 v[246:249], v[142:143], off
	global_load_dwordx4 v[234:237], v[142:143], off offset:528
	global_load_dwordx4 v[238:241], v[142:143], off offset:512
	v_readlane_b32 s18, v255, 6
	s_add_i32 s55, s55, 1
	s_nop 0
	v_mov_b32_e32 v2, s18
	ds_read_b32 v2, v2
	s_waitcnt lgkmcnt(0)
	v_readfirstlane_b32 s18, v2
	v_cmp_ge_i32_e32 vcc, s55, v2
	s_cmp_lt_i32 s55, s18
	s_cselect_b64 s[18:19], -1, 0
	s_cbranch_vccnz .LBB0_2957
	s_lshl_b32 s16, s55, 4
	s_add_i32 s16, s16, 0
	s_add_i32 s16, s16, 0x23200
	v_mov_b32_e32 v2, s16
	ds_read_b128 v[2:5], v2
	s_mov_b32 s56, s55
	s_waitcnt lgkmcnt(0)
	v_readfirstlane_b32 s17, v3
	v_readfirstlane_b32 s16, v2

.LBB0_2961:
	v_lshl_or_b32 v2, v23, 8, v164
	s_lshl_b32 s22, s31, 10
	v_add_u32_e32 v22, s22, v163
	v_ashrrev_i32_e32 v3, 31, v2
	ds_read_b32 v176, v22
	ds_read_b32 v178, v22 offset:64
	ds_read_b32 v180, v22 offset:128
	ds_read_b32 v182, v22 offset:192
	ds_read_b32 v184, v22 offset:512
	ds_read_b32 v186, v22 offset:576
	ds_read_b32 v188, v22 offset:640
	ds_read_b32 v190, v22 offset:704
	ds_read_b32 v192, v22 offset:13568
	ds_read_b32 v194, v22 offset:13632
	ds_read_b32 v196, v22 offset:13696
	ds_read_b32 v198, v22 offset:13760
	ds_read_b32 v200, v22 offset:14080
	ds_read_b32 v202, v22 offset:14144
	ds_read_b32 v204, v22 offset:14208
	ds_read_b32 v206, v22 offset:14272
	v_mov_b32_e32 v177, v99
	v_mov_b32_e32 v179, v99
	v_mov_b32_e32 v181, v99
	v_mov_b32_e32 v183, v99
	v_mov_b32_e32 v185, v99
	v_mov_b32_e32 v187, v99
	v_mov_b32_e32 v189, v99
	v_mov_b32_e32 v191, v99
	s_waitcnt lgkmcnt(0)
	v_lshlrev_b64 v[140:141], 11, v[176:177]
	v_lshl_add_u64 v[140:141], s[12:13], 0, v[140:141]
	v_lshl_add_u64 v[140:141], v[2:3], 1, v[140:141]
	v_lshlrev_b64 v[142:143], 11, v[178:179]
	v_lshl_add_u64 v[142:143], s[12:13], 0, v[142:143]
	v_lshl_add_u64 v[142:143], v[2:3], 1, v[142:143]
	v_lshlrev_b64 v[144:145], 11, v[180:181]
	v_lshl_add_u64 v[144:145], s[12:13], 0, v[144:145]
	v_lshl_add_u64 v[144:145], v[2:3], 1, v[144:145]
	v_lshlrev_b64 v[146:147], 11, v[182:183]
	v_lshl_add_u64 v[146:147], s[12:13], 0, v[146:147]
	v_lshl_add_u64 v[146:147], v[2:3], 1, v[146:147]
	v_lshlrev_b64 v[148:149], 11, v[184:185]
	v_lshl_add_u64 v[148:149], s[12:13], 0, v[148:149]
	v_lshl_add_u64 v[148:149], v[2:3], 1, v[148:149]
	v_lshlrev_b64 v[150:151], 11, v[186:187]
	v_lshl_add_u64 v[150:151], s[12:13], 0, v[150:151]
	v_lshl_add_u64 v[150:151], v[2:3], 1, v[150:151]
	v_lshlrev_b64 v[152:153], 11, v[188:189]
	v_lshl_add_u64 v[152:153], s[12:13], 0, v[152:153]
	v_lshl_add_u64 v[152:153], v[2:3], 1, v[152:153]
	v_lshlrev_b64 v[154:155], 11, v[190:191]
	v_lshl_add_u64 v[154:155], s[12:13], 0, v[154:155]
	v_lshl_add_u64 v[154:155], v[2:3], 1, v[154:155]
	v_pk_add_f32 v[138:139], v[138:139], v[248:249]
	v_pk_add_f32 v[136:137], v[136:137], v[246:247]
	v_pk_add_f32 v[134:135], v[134:135], v[244:245]
	v_pk_add_f32 v[132:133], v[132:133], v[242:243]
	v_pk_add_f32 v[130:131], v[130:131], v[240:241]
	v_pk_add_f32 v[128:129], v[128:129], v[238:239]
	v_pk_add_f32 v[126:127], v[126:127], v[236:237]
	v_pk_add_f32 v[124:125], v[124:125], v[234:235]
	v_pk_mul_f32 v[138:139], v[138:139], v[192:193] op_sel_hi:[1,0]
	v_pk_mul_f32 v[136:137], v[136:137], v[192:193] op_sel_hi:[1,0]
	v_pk_mul_f32 v[134:135], v[134:135], v[192:193] op_sel_hi:[1,0]
	v_pk_mul_f32 v[132:133], v[132:133], v[192:193] op_sel_hi:[1,0]
	v_pk_mul_f32 v[130:131], v[130:131], v[192:193] op_sel_hi:[1,0]
	v_pk_mul_f32 v[128:129], v[128:129], v[192:193] op_sel_hi:[1,0]
	v_pk_mul_f32 v[210:211], v[126:127], v[192:193] op_sel_hi:[1,0]
	v_pk_mul_f32 v[208:209], v[124:125], v[192:193] op_sel_hi:[1,0]
	v_cvt_pk_bf16_f32 v124, v136, v137
	v_cvt_pk_bf16_f32 v125, v138, v139
	v_cvt_pk_bf16_f32 v126, v132, v133
	v_cvt_pk_bf16_f32 v127, v134, v135
	v_cvt_pk_bf16_f32 v128, v128, v129
	v_cvt_pk_bf16_f32 v129, v130, v131
	v_cvt_pk_bf16_f32 v130, v208, v209
	v_cvt_pk_bf16_f32 v131, v210, v211
	v_pk_add_f32 v[122:123], v[122:123], v[248:249]
	v_pk_add_f32 v[120:121], v[120:121], v[246:247]
	v_pk_add_f32 v[118:119], v[118:119], v[244:245]
	v_pk_add_f32 v[116:117], v[116:117], v[242:243]
	v_pk_add_f32 v[114:115], v[114:115], v[240:241]
	v_pk_add_f32 v[112:113], v[112:113], v[238:239]
	v_pk_add_f32 v[110:111], v[110:111], v[236:237]
	v_pk_add_f32 v[108:109], v[108:109], v[234:235]
	v_pk_mul_f32 v[122:123], v[122:123], v[194:195] op_sel_hi:[1,0]
	v_pk_mul_f32 v[120:121], v[120:121], v[194:195] op_sel_hi:[1,0]
	v_pk_mul_f32 v[118:119], v[118:119], v[194:195] op_sel_hi:[1,0]
	v_pk_mul_f32 v[116:117], v[116:117], v[194:195] op_sel_hi:[1,0]
	v_pk_mul_f32 v[114:115], v[114:115], v[194:195] op_sel_hi:[1,0]
	v_pk_mul_f32 v[112:113], v[112:113], v[194:195] op_sel_hi:[1,0]
	v_pk_mul_f32 v[210:211], v[110:111], v[194:195] op_sel_hi:[1,0]
	v_pk_mul_f32 v[208:209], v[108:109], v[194:195] op_sel_hi:[1,0]
	v_cvt_pk_bf16_f32 v108, v120, v121
	v_cvt_pk_bf16_f32 v109, v122, v123
	v_cvt_pk_bf16_f32 v110, v116, v117
	v_cvt_pk_bf16_f32 v111, v118, v119
	v_cvt_pk_bf16_f32 v112, v112, v113
	v_cvt_pk_bf16_f32 v113, v114, v115
	v_cvt_pk_bf16_f32 v114, v208, v209
	v_cvt_pk_bf16_f32 v115, v210, v211
	v_pk_add_f32 v[106:107], v[106:107], v[248:249]
	v_pk_add_f32 v[104:105], v[104:105], v[246:247]
	v_pk_add_f32 v[102:103], v[102:103], v[244:245]
	v_pk_add_f32 v[100:101], v[100:101], v[242:243]
	v_pk_add_f32 v[94:95], v[94:95], v[240:241]
	v_pk_add_f32 v[92:93], v[92:93], v[238:239]
	v_pk_add_f32 v[90:91], v[90:91], v[236:237]
	v_pk_add_f32 v[88:89], v[88:89], v[234:235]
	v_pk_mul_f32 v[106:107], v[106:107], v[196:197] op_sel_hi:[1,0]
	v_pk_mul_f32 v[104:105], v[104:105], v[196:197] op_sel_hi:[1,0]
	v_pk_mul_f32 v[102:103], v[102:103], v[196:197] op_sel_hi:[1,0]
	v_pk_mul_f32 v[100:101], v[100:101], v[196:197] op_sel_hi:[1,0]
	v_pk_mul_f32 v[94:95], v[94:95], v[196:197] op_sel_hi:[1,0]
	v_pk_mul_f32 v[92:93], v[92:93], v[196:197] op_sel_hi:[1,0]
	v_pk_mul_f32 v[210:211], v[90:91], v[196:197] op_sel_hi:[1,0]
	v_pk_mul_f32 v[208:209], v[88:89], v[196:197] op_sel_hi:[1,0]
	v_cvt_pk_bf16_f32 v88, v104, v105
	v_cvt_pk_bf16_f32 v89, v106, v107
	v_cvt_pk_bf16_f32 v90, v100, v101
	v_cvt_pk_bf16_f32 v91, v102, v103
	v_cvt_pk_bf16_f32 v92, v92, v93
	v_cvt_pk_bf16_f32 v93, v94, v95
	v_cvt_pk_bf16_f32 v94, v208, v209
	v_cvt_pk_bf16_f32 v95, v210, v211
	v_pk_add_f32 v[86:87], v[86:87], v[248:249]
	v_pk_add_f32 v[84:85], v[84:85], v[246:247]
	v_pk_add_f32 v[82:83], v[82:83], v[244:245]
	v_pk_add_f32 v[80:81], v[80:81], v[242:243]
	v_pk_add_f32 v[78:79], v[78:79], v[240:241]
	v_pk_add_f32 v[76:77], v[76:77], v[238:239]
	v_pk_add_f32 v[74:75], v[74:75], v[236:237]
	v_pk_add_f32 v[72:73], v[72:73], v[234:235]
	v_pk_mul_f32 v[86:87], v[86:87], v[198:199] op_sel_hi:[1,0]
	v_pk_mul_f32 v[84:85], v[84:85], v[198:199] op_sel_hi:[1,0]
	v_pk_mul_f32 v[82:83], v[82:83], v[198:199] op_sel_hi:[1,0]
	v_pk_mul_f32 v[80:81], v[80:81], v[198:199] op_sel_hi:[1,0]
	v_pk_mul_f32 v[78:79], v[78:79], v[198:199] op_sel_hi:[1,0]
	v_pk_mul_f32 v[76:77], v[76:77], v[198:199] op_sel_hi:[1,0]
	v_pk_mul_f32 v[210:211], v[74:75], v[198:199] op_sel_hi:[1,0]
	v_pk_mul_f32 v[208:209], v[72:73], v[198:199] op_sel_hi:[1,0]
	v_cvt_pk_bf16_f32 v72, v84, v85
	v_cvt_pk_bf16_f32 v73, v86, v87
	v_cvt_pk_bf16_f32 v74, v80, v81
	v_cvt_pk_bf16_f32 v75, v82, v83
	v_cvt_pk_bf16_f32 v76, v76, v77
	v_cvt_pk_bf16_f32 v77, v78, v79
	v_cvt_pk_bf16_f32 v78, v208, v209
	v_cvt_pk_bf16_f32 v79, v210, v211
	v_pk_add_f32 v[70:71], v[70:71], v[248:249]
	v_pk_add_f32 v[68:69], v[68:69], v[246:247]
	v_pk_add_f32 v[66:67], v[66:67], v[244:245]
	v_pk_add_f32 v[64:65], v[64:65], v[242:243]
	v_pk_add_f32 v[62:63], v[62:63], v[240:241]
	v_pk_add_f32 v[60:61], v[60:61], v[238:239]
	v_pk_add_f32 v[58:59], v[58:59], v[236:237]
	v_pk_add_f32 v[56:57], v[56:57], v[234:235]
	v_pk_mul_f32 v[70:71], v[70:71], v[200:201] op_sel_hi:[1,0]
	v_pk_mul_f32 v[68:69], v[68:69], v[200:201] op_sel_hi:[1,0]
	v_pk_mul_f32 v[66:67], v[66:67], v[200:201] op_sel_hi:[1,0]
	v_pk_mul_f32 v[64:65], v[64:65], v[200:201] op_sel_hi:[1,0]
	v_pk_mul_f32 v[62:63], v[62:63], v[200:201] op_sel_hi:[1,0]
	v_pk_mul_f32 v[60:61], v[60:61], v[200:201] op_sel_hi:[1,0]
	v_pk_mul_f32 v[210:211], v[58:59], v[200:201] op_sel_hi:[1,0]
	v_pk_mul_f32 v[208:209], v[56:57], v[200:201] op_sel_hi:[1,0]
	v_cvt_pk_bf16_f32 v56, v68, v69
	v_cvt_pk_bf16_f32 v57, v70, v71
	v_cvt_pk_bf16_f32 v58, v64, v65
	v_cvt_pk_bf16_f32 v59, v66, v67
	v_cvt_pk_bf16_f32 v60, v60, v61
	v_cvt_pk_bf16_f32 v61, v62, v63
	v_cvt_pk_bf16_f32 v62, v208, v209
	v_cvt_pk_bf16_f32 v63, v210, v211
	v_pk_add_f32 v[54:55], v[54:55], v[248:249]
	v_pk_add_f32 v[52:53], v[52:53], v[246:247]
	v_pk_add_f32 v[50:51], v[50:51], v[244:245]
	v_pk_add_f32 v[48:49], v[48:49], v[242:243]
	v_pk_add_f32 v[46:47], v[46:47], v[240:241]
	v_pk_add_f32 v[44:45], v[44:45], v[238:239]
	v_pk_add_f32 v[42:43], v[42:43], v[236:237]
	v_pk_add_f32 v[40:41], v[40:41], v[234:235]
	v_pk_mul_f32 v[54:55], v[54:55], v[202:203] op_sel_hi:[1,0]
	v_pk_mul_f32 v[52:53], v[52:53], v[202:203] op_sel_hi:[1,0]
	v_pk_mul_f32 v[50:51], v[50:51], v[202:203] op_sel_hi:[1,0]
	v_pk_mul_f32 v[48:49], v[48:49], v[202:203] op_sel_hi:[1,0]
	v_pk_mul_f32 v[46:47], v[46:47], v[202:203] op_sel_hi:[1,0]
	v_pk_mul_f32 v[44:45], v[44:45], v[202:203] op_sel_hi:[1,0]
	v_pk_mul_f32 v[210:211], v[42:43], v[202:203] op_sel_hi:[1,0]
	v_pk_mul_f32 v[208:209], v[40:41], v[202:203] op_sel_hi:[1,0]
	v_cvt_pk_bf16_f32 v40, v52, v53
	v_cvt_pk_bf16_f32 v41, v54, v55
	v_cvt_pk_bf16_f32 v42, v48, v49
	v_cvt_pk_bf16_f32 v43, v50, v51
	v_cvt_pk_bf16_f32 v44, v44, v45
	v_cvt_pk_bf16_f32 v45, v46, v47
	v_cvt_pk_bf16_f32 v46, v208, v209
	v_cvt_pk_bf16_f32 v47, v210, v211
	v_pk_add_f32 v[38:39], v[38:39], v[248:249]
	v_pk_add_f32 v[36:37], v[36:37], v[246:247]
	v_pk_add_f32 v[34:35], v[34:35], v[244:245]
	v_pk_add_f32 v[32:33], v[32:33], v[242:243]
	v_pk_add_f32 v[30:31], v[30:31], v[240:241]
	v_pk_add_f32 v[28:29], v[28:29], v[238:239]
	v_pk_add_f32 v[26:27], v[26:27], v[236:237]
	v_pk_add_f32 v[24:25], v[24:25], v[234:235]
	v_pk_mul_f32 v[38:39], v[38:39], v[204:205] op_sel_hi:[1,0]
	v_pk_mul_f32 v[36:37], v[36:37], v[204:205] op_sel_hi:[1,0]
	v_pk_mul_f32 v[34:35], v[34:35], v[204:205] op_sel_hi:[1,0]
	v_pk_mul_f32 v[32:33], v[32:33], v[204:205] op_sel_hi:[1,0]
	v_pk_mul_f32 v[30:31], v[30:31], v[204:205] op_sel_hi:[1,0]
	v_pk_mul_f32 v[28:29], v[28:29], v[204:205] op_sel_hi:[1,0]
	v_pk_mul_f32 v[210:211], v[26:27], v[204:205] op_sel_hi:[1,0]
	v_pk_mul_f32 v[208:209], v[24:25], v[204:205] op_sel_hi:[1,0]
	v_cvt_pk_bf16_f32 v24, v36, v37
	v_cvt_pk_bf16_f32 v25, v38, v39
	v_cvt_pk_bf16_f32 v26, v32, v33
	v_cvt_pk_bf16_f32 v27, v34, v35
	v_cvt_pk_bf16_f32 v28, v28, v29
	v_cvt_pk_bf16_f32 v29, v30, v31
	v_cvt_pk_bf16_f32 v30, v208, v209
	v_cvt_pk_bf16_f32 v31, v210, v211
	v_pk_add_f32 v[20:21], v[20:21], v[248:249]
	v_pk_add_f32 v[18:19], v[18:19], v[246:247]
	v_pk_add_f32 v[16:17], v[16:17], v[244:245]
	v_pk_add_f32 v[14:15], v[14:15], v[242:243]
	v_pk_add_f32 v[12:13], v[12:13], v[240:241]
	v_pk_add_f32 v[10:11], v[10:11], v[238:239]
	v_pk_add_f32 v[8:9], v[8:9], v[236:237]
	v_pk_add_f32 v[6:7], v[6:7], v[234:235]
	v_pk_mul_f32 v[20:21], v[20:21], v[206:207] op_sel_hi:[1,0]
	v_pk_mul_f32 v[18:19], v[18:19], v[206:207] op_sel_hi:[1,0]
	v_pk_mul_f32 v[16:17], v[16:17], v[206:207] op_sel_hi:[1,0]
	v_pk_mul_f32 v[14:15], v[14:15], v[206:207] op_sel_hi:[1,0]
	v_pk_mul_f32 v[12:13], v[12:13], v[206:207] op_sel_hi:[1,0]
	v_pk_mul_f32 v[10:11], v[10:11], v[206:207] op_sel_hi:[1,0]
	v_pk_mul_f32 v[210:211], v[8:9], v[206:207] op_sel_hi:[1,0]
	v_pk_mul_f32 v[208:209], v[6:7], v[206:207] op_sel_hi:[1,0]
	v_cvt_pk_bf16_f32 v6, v18, v19
	v_cvt_pk_bf16_f32 v7, v20, v21
	v_cvt_pk_bf16_f32 v8, v14, v15
	v_cvt_pk_bf16_f32 v9, v16, v17
	v_cvt_pk_bf16_f32 v10, v10, v11
	v_cvt_pk_bf16_f32 v11, v12, v13
	v_cvt_pk_bf16_f32 v12, v208, v209
	v_cvt_pk_bf16_f32 v13, v210, v211
	s_waitcnt vmcnt(0)
	v_cmp_lt_i32_e32 vcc, -1, v176
	s_and_saveexec_b64 s[38:39], vcc
	s_cbranch_execz .Lepidn_skip_0
	global_store_dwordx4 v[140:141], v[124:127], off
	global_store_dwordx4 v[140:141], v[128:131], off offset:256
.Lepidn_skip_0:
	s_or_b64 exec, exec, s[38:39]
	v_cmp_lt_i32_e32 vcc, -1, v178
	s_and_saveexec_b64 s[38:39], vcc
	s_cbranch_execz .Lepidn_skip_1
	global_store_dwordx4 v[142:143], v[108:111], off
	global_store_dwordx4 v[142:143], v[112:115], off offset:256
.Lepidn_skip_1:
	s_or_b64 exec, exec, s[38:39]
	v_cmp_lt_i32_e32 vcc, -1, v180
	s_and_saveexec_b64 s[38:39], vcc
	s_cbranch_execz .Lepidn_skip_2
	global_store_dwordx4 v[144:145], v[88:91], off
	global_store_dwordx4 v[144:145], v[92:95], off offset:256
.Lepidn_skip_2:
	s_or_b64 exec, exec, s[38:39]
	v_cmp_lt_i32_e32 vcc, -1, v182
	s_and_saveexec_b64 s[38:39], vcc
	s_cbranch_execz .Lepidn_skip_3
	global_store_dwordx4 v[146:147], v[72:75], off
	global_store_dwordx4 v[146:147], v[76:79], off offset:256
.Lepidn_skip_3:
	s_or_b64 exec, exec, s[38:39]
	v_cmp_lt_i32_e32 vcc, -1, v184
	s_and_saveexec_b64 s[38:39], vcc
	s_cbranch_execz .Lepidn_skip_4
	global_store_dwordx4 v[148:149], v[56:59], off
	global_store_dwordx4 v[148:149], v[60:63], off offset:256
.Lepidn_skip_4:
	s_or_b64 exec, exec, s[38:39]
	v_cmp_lt_i32_e32 vcc, -1, v186
	s_and_saveexec_b64 s[38:39], vcc
	s_cbranch_execz .Lepidn_skip_5
	global_store_dwordx4 v[150:151], v[40:43], off
	global_store_dwordx4 v[150:151], v[44:47], off offset:256
.Lepidn_skip_5:
	s_or_b64 exec, exec, s[38:39]
	v_cmp_lt_i32_e32 vcc, -1, v188
	s_and_saveexec_b64 s[38:39], vcc
	s_cbranch_execz .Lepidn_skip_6
	global_store_dwordx4 v[152:153], v[24:27], off
	global_store_dwordx4 v[152:153], v[28:31], off offset:256
.Lepidn_skip_6:
	s_or_b64 exec, exec, s[38:39]
	v_cmp_lt_i32_e32 vcc, -1, v190
	s_and_saveexec_b64 s[38:39], vcc
	s_cbranch_execz .LBB0_2977
	global_store_dwordx4 v[154:155], v[6:9], off
	global_store_dwordx4 v[154:155], v[10:13], off offset:256

	.amdhsa_kernel _ZN2mk4megaENS_4ArgsE
		.amdhsa_group_segment_fixed_size 12800
		.amdhsa_private_segment_fixed_size 0
		.amdhsa_kernarg_size 544
		.amdhsa_user_sgpr_count 2
		.amdhsa_user_sgpr_dispatch_ptr 0
		.amdhsa_user_sgpr_queue_ptr 0
		.amdhsa_user_sgpr_kernarg_segment_ptr 1
		.amdhsa_user_sgpr_dispatch_id 0
		.amdhsa_user_sgpr_kernarg_preload_length 0
		.amdhsa_user_sgpr_kernarg_preload_offset 0
		.amdhsa_user_sgpr_private_segment_size 0
		.amdhsa_uses_dynamic_stack 0
		.amdhsa_enable_private_segment 0
		.amdhsa_system_sgpr_workgroup_id_x 1
		.amdhsa_system_sgpr_workgroup_id_y 0
		.amdhsa_system_sgpr_workgroup_id_z 0
		.amdhsa_system_sgpr_workgroup_info 0
		.amdhsa_system_vgpr_workitem_id 0
		.amdhsa_next_free_vgpr 256
		.amdhsa_next_free_sgpr 102
		.amdhsa_accum_offset 256
		.amdhsa_reserve_vcc 1
		.amdhsa_float_round_mode_32 0
		.amdhsa_float_round_mode_16_64 0
		.amdhsa_float_denorm_mode_32 3
		.amdhsa_float_denorm_mode_16_64 3
		.amdhsa_dx10_clamp 1
		.amdhsa_ieee_mode 1
		.amdhsa_fp16_overflow 0
		.amdhsa_tg_split 0
		.amdhsa_exception_fp_ieee_invalid_op 0
		.amdhsa_exception_fp_denorm_src 0
		.amdhsa_exception_fp_ieee_div_zero 0
		.amdhsa_exception_fp_ieee_overflow 0
		.amdhsa_exception_fp_ieee_underflow 0
		.amdhsa_exception_fp_ieee_inexact 0
		.amdhsa_exception_int_div_zero 0
	.end_amdhsa_kernel

amdhsa.kernels:
  - .agpr_count:     0
    .args:
      - .offset:         0
        .size:           288
        .value_kind:     by_value
      - .offset:         288
        .size:           4
        .value_kind:     hidden_block_count_x
      - .offset:         292
        .size:           4
        .value_kind:     hidden_block_count_y
      - .offset:         296
        .size:           4
        .value_kind:     hidden_block_count_z
      - .offset:         300
        .size:           2
        .value_kind:     hidden_group_size_x
      - .offset:         302
        .size:           2
        .value_kind:     hidden_group_size_y
      - .offset:         304
        .size:           2
        .value_kind:     hidden_group_size_z
      - .offset:         306
        .size:           2
        .value_kind:     hidden_remainder_x
      - .offset:         308
        .size:           2
        .value_kind:     hidden_remainder_y
      - .offset:         310
        .size:           2
        .value_kind:     hidden_remainder_z
      - .offset:         328
        .size:           8
        .value_kind:     hidden_global_offset_x
      - .offset:         336
        .size:           8
        .value_kind:     hidden_global_offset_y
      - .offset:         344
        .size:           8
        .value_kind:     hidden_global_offset_z
      - .offset:         352
        .size:           2
        .value_kind:     hidden_grid_dims
      - .offset:         408
        .size:           4
        .value_kind:     hidden_dynamic_lds_size
    .group_segment_fixed_size: 12800
    .kernarg_segment_align: 8
    .kernarg_segment_size: 544
    .language:       OpenCL C
    .language_version:
      - 2
      - 0
    .max_flat_workgroup_size: 512
    .name:           _ZN2mk4megaENS_4ArgsE
    .private_segment_fixed_size: 0
    .sgpr_count:     108
    .sgpr_spill_count: 319
    .symbol:         _ZN2mk4megaENS_4ArgsE.kd
    .uniform_work_group_size: 1
    .uses_dynamic_stack: false
    .vgpr_count:     256
    .vgpr_spill_count: 0
    .wavefront_size: 64
